# SwiGLU8 epilogues of ph7 (bf16+fp8) and MoE ph15/ph17 regenerated for ILP (packed f32, no copies); ph7 row-scale partial-sum loads hoisted before the K-loop; bit-identical
# speedup vs baseline: 1.0070x; 1.0070x over previous
.LBB0_815:
	s_ashr_i32 s45, s44, 31
	s_lshl_b64 s[48:49], s[44:45], 19
	s_add_u32 s48, s8, s48
	s_addc_u32 s49, s10, s49
	s_ashr_i32 s43, s42, 31
	s_lshl_b64 s[50:51], s[42:43], 19
	s_add_u32 s50, s11, s50
	s_addc_u32 s51, s12, s51
	s_andn2_b64 vcc, exec, s[34:35]
	s_cbranch_vccnz .LBB0_823
	v_lshl_add_u32 v156, s52, 8, v149
	v_ashrrev_i32_e32 v157, 31, v156
	v_lshl_add_u64 v[158:159], v[156:157], 2, v[136:137]
	global_load_dword v244, v[158:159], off
	global_load_dword v245, v[158:159], off offset:64
	global_load_dword v246, v[158:159], off offset:128
	global_load_dword v247, v[158:159], off offset:192
	global_load_dword v248, v[158:159], off offset:512
	global_load_dword v249, v[158:159], off offset:576
	global_load_dword v250, v[158:159], off offset:640
	global_load_dword v251, v[158:159], off offset:704
	s_and_b64 s[60:61], s[46:47], exec
	s_cselect_b32 s43, s49, s55
	s_cselect_b32 s45, s48, s54
	s_cselect_b32 s64, s51, s59
	s_cselect_b32 s65, s50, s58
	s_add_u32 s66, s58, 0x100
	s_addc_u32 s68, s59, 0
	s_add_u32 s54, s54, 0x40080
	v_mov_b32_e32 v34, 0
	v_mov_b32_e32 v1, 0x3ecc95a3
	s_addc_u32 s55, s55, 0
	s_mov_b32 s58, 0
	v_mov_b32_e32 v35, v34
	v_mov_b32_e32 v36, v34
	v_mov_b32_e32 v37, v34
	v_mov_b32_e32 v42, v34
	v_mov_b32_e32 v43, v34
	v_mov_b32_e32 v44, v34
	v_mov_b32_e32 v45, v34
	v_mov_b32_e32 v50, v34
	v_mov_b32_e32 v51, v34
	v_mov_b32_e32 v52, v34
	v_mov_b32_e32 v53, v34
	v_mov_b32_e32 v58, v34
	v_mov_b32_e32 v59, v34
	v_mov_b32_e32 v60, v34
	v_mov_b32_e32 v61, v34
	v_mov_b32_e32 v6, v34
	v_mov_b32_e32 v7, v34
	v_mov_b32_e32 v8, v34
	v_mov_b32_e32 v9, v34
	v_mov_b32_e32 v14, v34
	v_mov_b32_e32 v15, v34
	v_mov_b32_e32 v16, v34
	v_mov_b32_e32 v17, v34
	v_mov_b32_e32 v22, v34
	v_mov_b32_e32 v23, v34
	v_mov_b32_e32 v24, v34
	v_mov_b32_e32 v25, v34
	v_mov_b32_e32 v30, v34
	v_mov_b32_e32 v31, v34
	v_mov_b32_e32 v32, v34
	v_mov_b32_e32 v33, v34
	v_mov_b32_e32 v38, v34
	v_mov_b32_e32 v39, v34
	v_mov_b32_e32 v40, v34
	v_mov_b32_e32 v41, v34
	v_mov_b32_e32 v46, v34
	v_mov_b32_e32 v47, v34
	v_mov_b32_e32 v48, v34
	v_mov_b32_e32 v49, v34
	v_mov_b32_e32 v54, v34
	v_mov_b32_e32 v55, v34
	v_mov_b32_e32 v56, v34
	v_mov_b32_e32 v57, v34
	v_mov_b32_e32 v62, v34
	v_mov_b32_e32 v63, v34
	v_mov_b32_e32 v64, v34
	v_mov_b32_e32 v65, v34
	v_mov_b32_e32 v66, v34
	v_mov_b32_e32 v67, v34
	v_mov_b32_e32 v68, v34
	v_mov_b32_e32 v69, v34
	v_mov_b32_e32 v74, v34
	v_mov_b32_e32 v75, v34
	v_mov_b32_e32 v76, v34
	v_mov_b32_e32 v77, v34
	v_mov_b32_e32 v82, v34
	v_mov_b32_e32 v83, v34
	v_mov_b32_e32 v84, v34
	v_mov_b32_e32 v85, v34
	v_mov_b32_e32 v90, v34
	v_mov_b32_e32 v91, v34
	v_mov_b32_e32 v92, v34
	v_mov_b32_e32 v93, v34
	v_mov_b32_e32 v98, v34
	v_mov_b32_e32 v99, v34
	v_mov_b32_e32 v100, v34
	v_mov_b32_e32 v101, v34
	v_mov_b32_e32 v106, v34
	v_mov_b32_e32 v107, v34
	v_mov_b32_e32 v108, v34
	v_mov_b32_e32 v109, v34
	v_mov_b32_e32 v114, v34
	v_mov_b32_e32 v115, v34
	v_mov_b32_e32 v116, v34
	v_mov_b32_e32 v117, v34
	v_mov_b32_e32 v122, v34
	v_mov_b32_e32 v123, v34
	v_mov_b32_e32 v124, v34
	v_mov_b32_e32 v125, v34
	v_mov_b32_e32 v70, v34
	v_mov_b32_e32 v71, v34
	v_mov_b32_e32 v72, v34
	v_mov_b32_e32 v73, v34
	v_mov_b32_e32 v78, v34
	v_mov_b32_e32 v79, v34
	v_mov_b32_e32 v80, v34
	v_mov_b32_e32 v81, v34
	v_mov_b32_e32 v86, v34
	v_mov_b32_e32 v87, v34
	v_mov_b32_e32 v88, v34
	v_mov_b32_e32 v89, v34
	v_mov_b32_e32 v94, v34
	v_mov_b32_e32 v95, v34
	v_mov_b32_e32 v96, v34
	v_mov_b32_e32 v97, v34
	v_mov_b32_e32 v102, v34
	v_mov_b32_e32 v103, v34
	v_mov_b32_e32 v104, v34
	v_mov_b32_e32 v105, v34
	v_mov_b32_e32 v110, v34
	v_mov_b32_e32 v111, v34
	v_mov_b32_e32 v112, v34
	v_mov_b32_e32 v113, v34
	v_mov_b32_e32 v118, v34
	v_mov_b32_e32 v119, v34
	v_mov_b32_e32 v120, v34
	v_mov_b32_e32 v121, v34
	v_mov_b32_e32 v126, v34
	v_mov_b32_e32 v127, v34
	v_mov_b32_e32 v128, v34
	v_mov_b32_e32 v129, v34
	v_mov_b32_e32 v26, v34
	v_mov_b32_e32 v27, v34
	v_mov_b32_e32 v28, v34
	v_mov_b32_e32 v29, v34
	v_mov_b32_e32 v18, v34
	v_mov_b32_e32 v19, v34
	v_mov_b32_e32 v20, v34
	v_mov_b32_e32 v21, v34
	v_mov_b32_e32 v10, v34
	v_mov_b32_e32 v11, v34
	v_mov_b32_e32 v12, v34
	v_mov_b32_e32 v13, v34
	v_mov_b32_e32 v2, v34
	v_mov_b32_e32 v3, v34
	v_mov_b32_e32 v4, v34
	v_mov_b32_e32 v5, v34

.LBB0_820:
	v_xor_b32_e32 v218, 16, v231
	v_and_b32_e32 v216, 64, v231
	v_add_u32_e32 v216, 64, v216
	v_xor_b32_e32 v217, 32, v231
	v_cmp_lt_i32_e32 vcc, v218, v216
	v_mov_b32_e32 v142, 0xbfb8aa3b
	v_mov_b32_e32 v143, 1.0
	v_cndmask_b32_e32 v218, v231, v218, vcc
	v_cmp_lt_i32_e32 vcc, v217, v216
	v_lshlrev_b32_e32 v218, 2, v218
	v_mov_b32_e32 v144, 0x41000000
	v_cndmask_b32_e32 v217, v231, v217, vcc
	v_lshlrev_b32_e32 v217, 2, v217
	ds_bpermute_b32 v156, v218, v244
	ds_bpermute_b32 v157, v218, v245
	ds_bpermute_b32 v158, v218, v246
	ds_bpermute_b32 v159, v218, v247
	ds_bpermute_b32 v160, v218, v248
	ds_bpermute_b32 v161, v218, v249
	ds_bpermute_b32 v162, v218, v250
	ds_bpermute_b32 v163, v218, v251
	v_lshl_add_u32 v221, s52, 8, v149
	v_lshl_or_b32 v220, s63, 7, v153
	v_mad_u32_u24 v219, v221, s33, v220
	s_waitcnt lgkmcnt(7)
	v_add_f32_e32 v244, v244, v156
	ds_bpermute_b32 v156, v217, v244
	s_waitcnt lgkmcnt(7)
	v_add_f32_e32 v245, v245, v157
	ds_bpermute_b32 v157, v217, v245
	s_waitcnt lgkmcnt(7)
	v_add_f32_e32 v246, v246, v158
	ds_bpermute_b32 v158, v217, v246
	s_waitcnt lgkmcnt(7)
	v_add_f32_e32 v247, v247, v159
	ds_bpermute_b32 v159, v217, v247
	s_waitcnt lgkmcnt(7)
	v_add_f32_e32 v248, v248, v160
	ds_bpermute_b32 v160, v217, v248
	s_waitcnt lgkmcnt(7)
	v_add_f32_e32 v249, v249, v161
	ds_bpermute_b32 v161, v217, v249
	s_waitcnt lgkmcnt(7)
	v_add_f32_e32 v250, v250, v162
	ds_bpermute_b32 v162, v217, v250
	s_waitcnt lgkmcnt(7)
	v_add_f32_e32 v251, v251, v163
	ds_bpermute_b32 v163, v217, v251
	s_waitcnt lgkmcnt(7)
	v_add_f32_e32 v244, v244, v156
	v_fmamk_f32 v244, v244, 0x3a800000, v224
	s_waitcnt lgkmcnt(6)
	v_add_f32_e32 v245, v245, v157
	v_fmamk_f32 v245, v245, 0x3a800000, v224
	s_waitcnt lgkmcnt(5)
	v_add_f32_e32 v246, v246, v158
	v_fmamk_f32 v246, v246, 0x3a800000, v224
	s_waitcnt lgkmcnt(4)
	v_add_f32_e32 v247, v247, v159
	v_fmamk_f32 v247, v247, 0x3a800000, v224
	s_waitcnt lgkmcnt(3)
	v_add_f32_e32 v248, v248, v160
	v_fmamk_f32 v248, v248, 0x3a800000, v224
	s_waitcnt lgkmcnt(2)
	v_add_f32_e32 v249, v249, v161
	v_fmamk_f32 v249, v249, 0x3a800000, v224
	s_waitcnt lgkmcnt(1)
	v_add_f32_e32 v250, v250, v162
	v_fmamk_f32 v250, v250, 0x3a800000, v224
	s_waitcnt lgkmcnt(0)
	v_add_f32_e32 v251, v251, v163
	v_fmamk_f32 v251, v251, 0x3a800000, v224
	v_rsq_f32_e32 v244, v244
	v_rsq_f32_e32 v245, v245
	v_rsq_f32_e32 v246, v246
	v_rsq_f32_e32 v247, v247
	v_rsq_f32_e32 v248, v248
	v_rsq_f32_e32 v249, v249
	v_rsq_f32_e32 v250, v250
	v_rsq_f32_e32 v251, v251
	v_pk_mul_f32 v[156:157], v[126:127], v[244:245] op_sel_hi:[1,0]
	v_pk_mul_f32 v[158:159], v[128:129], v[244:245] op_sel_hi:[1,0]
	v_pk_mul_f32 v[160:161], v[118:119], v[244:245] op_sel_hi:[1,0]
	v_pk_mul_f32 v[162:163], v[156:157], v[142:143] op_sel_hi:[1,0]
	v_pk_mul_f32 v[170:171], v[158:159], v[142:143] op_sel_hi:[1,0]
	v_pk_mul_f32 v[172:173], v[160:161], v[142:143] op_sel_hi:[1,0]
	v_exp_f32_e32 v162, v162
	v_pk_mul_f32 v[174:175], v[120:121], v[244:245] op_sel_hi:[1,0]
	v_exp_f32_e32 v170, v170
	v_pk_mul_f32 v[176:177], v[110:111], v[244:245] op_sel:[0,1] op_sel_hi:[1,1]
	v_exp_f32_e32 v172, v172
	v_pk_mul_f32 v[178:179], v[174:175], v[142:143] op_sel_hi:[1,0]
	v_pk_mul_f32 v[180:181], v[176:177], v[142:143] op_sel_hi:[1,0]
	v_pk_mul_f32 v[182:183], v[112:113], v[244:245] op_sel:[0,1] op_sel_hi:[1,1]
	v_exp_f32_e32 v178, v178
	v_pk_mul_f32 v[184:185], v[102:103], v[244:245] op_sel:[0,1] op_sel_hi:[1,1]
	v_exp_f32_e32 v163, v163
	v_pk_mul_f32 v[186:187], v[182:183], v[142:143] op_sel_hi:[1,0]
	v_exp_f32_e32 v171, v171
	v_pk_mul_f32 v[188:189], v[184:185], v[142:143] op_sel_hi:[1,0]
	v_exp_f32_e32 v173, v173
	v_pk_mul_f32 v[190:191], v[104:105], v[244:245] op_sel:[0,1] op_sel_hi:[1,1]
	v_exp_f32_e32 v179, v179
	v_pk_mul_f32 v[192:193], v[94:95], v[246:247] op_sel_hi:[1,0]
	v_exp_f32_e32 v180, v180
	v_pk_add_f32 v[162:163], v[162:163], v[142:143] op_sel:[0,1] op_sel_hi:[1,1]
	v_exp_f32_e32 v186, v186
	v_pk_mul_f32 v[194:195], v[190:191], v[142:143] op_sel_hi:[1,0]
	v_exp_f32_e32 v188, v188
	v_pk_add_f32 v[170:171], v[170:171], v[142:143] op_sel:[0,1] op_sel_hi:[1,1]
	v_rcp_f32_e32 v162, v162
	v_pk_add_f32 v[172:173], v[172:173], v[142:143] op_sel:[0,1] op_sel_hi:[1,1]
	v_exp_f32_e32 v194, v194
	v_pk_add_f32 v[178:179], v[178:179], v[142:143] op_sel:[0,1] op_sel_hi:[1,1]
	v_rcp_f32_e32 v170, v170
	v_pk_mul_f32 v[196:197], v[192:193], v[142:143] op_sel_hi:[1,0]
	v_rcp_f32_e32 v172, v172
	v_pk_mul_f32 v[198:199], v[96:97], v[246:247] op_sel_hi:[1,0]
	v_exp_f32_e32 v181, v181
	v_pk_mul_f32 v[200:201], v[86:87], v[246:247] op_sel_hi:[1,0]
	v_rcp_f32_e32 v178, v178
	v_pk_mul_f32 v[202:203], v[198:199], v[142:143] op_sel_hi:[1,0]
	v_exp_f32_e32 v187, v187
	v_pk_mul_f32 v[204:205], v[200:201], v[142:143] op_sel_hi:[1,0]
	v_exp_f32_e32 v189, v189
	v_pk_mul_f32 v[206:207], v[88:89], v[246:247] op_sel_hi:[1,0]
	v_rcp_f32_e32 v163, v163
	v_pk_add_f32 v[180:181], v[180:181], v[142:143] op_sel:[0,1] op_sel_hi:[1,1]
	v_exp_f32_e32 v195, v195
	v_pk_mul_f32 v[208:209], v[206:207], v[142:143] op_sel_hi:[1,0]
	v_exp_f32_e32 v196, v196
	v_pk_add_f32 v[186:187], v[186:187], v[142:143] op_sel:[0,1] op_sel_hi:[1,1]
	v_rcp_f32_e32 v171, v171
	v_pk_add_f32 v[188:189], v[188:189], v[142:143] op_sel:[0,1] op_sel_hi:[1,1]
	v_rcp_f32_e32 v173, v173
	v_pk_mul_f32 v[210:211], v[122:123], v[244:245] op_sel_hi:[1,0]
	v_exp_f32_e32 v202, v202
	v_pk_add_f32 v[194:195], v[194:195], v[142:143] op_sel:[0,1] op_sel_hi:[1,1]
	v_exp_f32_e32 v204, v204
	v_pk_mul_f32 v[212:213], v[78:79], v[246:247] op_sel:[0,1] op_sel_hi:[1,1]
	v_rcp_f32_e32 v179, v179
	v_pk_mul_f32 v[210:211], v[210:211], v[156:157]
	v_rcp_f32_e32 v180, v180
	v_pk_mul_f32 v[156:157], v[124:125], v[244:245] op_sel_hi:[1,0]
	v_exp_f32_e32 v208, v208
	v_pk_mul_f32 v[210:211], v[210:211], v[162:163]
	v_rcp_f32_e32 v186, v186
	v_pk_mul_f32 v[162:163], v[114:115], v[244:245] op_sel_hi:[1,0]
	v_rcp_f32_e32 v188, v188
	v_pk_mul_f32 v[210:211], v[210:211], v[144:145] op_sel_hi:[1,0]
	v_exp_f32_e32 v197, v197
	v_pk_mul_f32 v[214:215], v[212:213], v[142:143] op_sel_hi:[1,0]
	v_rcp_f32_e32 v194, v194
	v_med3_f32 v210, v210, s87, v227
	v_exp_f32_e32 v203, v203
	v_pk_mul_f32 v[156:157], v[156:157], v[158:159]
	v_exp_f32_e32 v205, v205
	v_pk_mul_f32 v[158:159], v[80:81], v[246:247] op_sel:[0,1] op_sel_hi:[1,1]
	v_pk_mul_f32 v[156:157], v[156:157], v[170:171]
	v_pk_mul_f32 v[170:171], v[70:71], v[246:247] op_sel:[0,1] op_sel_hi:[1,1]
	v_pk_mul_f32 v[162:163], v[162:163], v[160:161]
	v_pk_mul_f32 v[156:157], v[156:157], v[144:145] op_sel_hi:[1,0]
	v_pk_mul_f32 v[160:161], v[116:117], v[244:245] op_sel_hi:[1,0]
	v_pk_mul_f32 v[162:163], v[162:163], v[172:173]
	v_rcp_f32_e32 v181, v181
	v_pk_mul_f32 v[172:173], v[158:159], v[142:143] op_sel_hi:[1,0]
	v_pk_mul_f32 v[162:163], v[162:163], v[144:145] op_sel_hi:[1,0]
	v_exp_f32_e32 v209, v209
	v_med3_f32 v211, v211, s87, v227
	v_exp_f32_e32 v214, v214
	v_med3_f32 v156, v156, s87, v227
	v_med3_f32 v162, v162, s87, v227
	v_pk_mul_f32 v[160:161], v[160:161], v[174:175]
	v_pk_mul_f32 v[174:175], v[170:171], v[142:143] op_sel_hi:[1,0]
	v_rcp_f32_e32 v187, v187
	v_pk_mul_f32 v[160:161], v[160:161], v[178:179]
	v_pk_mul_f32 v[178:179], v[72:73], v[246:247] op_sel:[0,1] op_sel_hi:[1,1]
	v_rcp_f32_e32 v189, v189
	v_pk_mul_f32 v[160:161], v[160:161], v[144:145] op_sel_hi:[1,0]
	v_pk_add_f32 v[196:197], v[196:197], v[142:143] op_sel:[0,1] op_sel_hi:[1,1]
	v_exp_f32_e32 v172, v172
	v_cvt_pk_fp8_f32 v210, v210, v211
	v_exp_f32_e32 v174, v174
	v_med3_f32 v157, v157, s87, v227
	v_med3_f32 v163, v163, s87, v227
	v_med3_f32 v160, v160, s87, v227
	v_rcp_f32_e32 v195, v195
	v_pk_add_f32 v[202:203], v[202:203], v[142:143] op_sel:[0,1] op_sel_hi:[1,1]
	v_rcp_f32_e32 v196, v196
	v_pk_add_f32 v[204:205], v[204:205], v[142:143] op_sel:[0,1] op_sel_hi:[1,1]
	v_cvt_pk_fp8_f32 v210, v156, v157 op_sel:[0,0,1]
	v_pk_mul_f32 v[156:157], v[178:179], v[142:143] op_sel_hi:[1,0]
	v_cvt_pk_fp8_f32 v211, v162, v163
	v_pk_mul_f32 v[162:163], v[106:107], v[244:245] op_sel:[0,1] op_sel_hi:[1,1]
	v_exp_f32_e32 v156, v156
	v_med3_f32 v161, v161, s87, v227
	v_rcp_f32_e32 v202, v202
	v_pk_add_f32 v[208:209], v[208:209], v[142:143] op_sel:[0,1] op_sel_hi:[1,1]
	v_rcp_f32_e32 v204, v204
	v_pk_mul_f32 v[162:163], v[162:163], v[176:177]
	v_exp_f32_e32 v215, v215
	v_pk_mul_f32 v[176:177], v[62:63], v[248:249] op_sel_hi:[1,0]
	v_pk_mul_f32 v[162:163], v[162:163], v[180:181]
	v_pk_mul_f32 v[180:181], v[108:109], v[244:245] op_sel:[0,1] op_sel_hi:[1,1]
	v_cvt_pk_fp8_f32 v211, v160, v161 op_sel:[0,0,1]
	v_pk_mul_f32 v[162:163], v[162:163], v[144:145] op_sel_hi:[1,0]
	v_pk_mul_f32 v[160:161], v[98:99], v[244:245] op_sel:[0,1] op_sel_hi:[1,1]
	v_rcp_f32_e32 v208, v208
	v_med3_f32 v162, v162, s87, v227
	v_exp_f32_e32 v173, v173
	v_pk_mul_f32 v[180:181], v[180:181], v[182:183]
	v_exp_f32_e32 v175, v175
	v_pk_mul_f32 v[182:183], v[176:177], v[142:143] op_sel_hi:[1,0]
	v_pk_mul_f32 v[180:181], v[180:181], v[186:187]
	v_pk_mul_f32 v[186:187], v[64:65], v[248:249] op_sel_hi:[1,0]
	v_pk_mul_f32 v[160:161], v[160:161], v[184:185]
	v_pk_mul_f32 v[184:185], v[54:55], v[248:249] op_sel_hi:[1,0]
	v_pk_mul_f32 v[180:181], v[180:181], v[144:145] op_sel_hi:[1,0]
	v_pk_mul_f32 v[160:161], v[160:161], v[188:189]
	v_pk_mul_f32 v[188:189], v[100:101], v[244:245] op_sel:[0,1] op_sel_hi:[1,1]
	v_rcp_f32_e32 v197, v197
	v_pk_mul_f32 v[160:161], v[160:161], v[144:145] op_sel_hi:[1,0]
	global_store_dwordx2 v219, v[210:211], s[26:27]
	v_exp_f32_e32 v157, v157
	v_pk_mul_f32 v[210:211], v[186:187], v[142:143] op_sel_hi:[1,0]
	v_exp_f32_e32 v182, v182
	v_med3_f32 v163, v163, s87, v227
	v_med3_f32 v180, v180, s87, v227
	v_med3_f32 v160, v160, s87, v227
	v_pk_mul_f32 v[188:189], v[188:189], v[190:191]
	v_pk_mul_f32 v[190:191], v[184:185], v[142:143] op_sel_hi:[1,0]
	v_rcp_f32_e32 v203, v203
	v_pk_mul_f32 v[188:189], v[188:189], v[194:195]
	v_pk_mul_f32 v[194:195], v[56:57], v[248:249] op_sel_hi:[1,0]
	v_rcp_f32_e32 v205, v205
	v_pk_mul_f32 v[188:189], v[188:189], v[144:145] op_sel_hi:[1,0]
	v_pk_add_f32 v[214:215], v[214:215], v[142:143] op_sel:[0,1] op_sel_hi:[1,1]
	v_exp_f32_e32 v210, v210
	v_cvt_pk_fp8_f32 v162, v162, v163
	v_exp_f32_e32 v190, v190
	v_med3_f32 v181, v181, s87, v227
	v_med3_f32 v161, v161, s87, v227
	v_med3_f32 v188, v188, s87, v227
	v_rcp_f32_e32 v209, v209
	v_pk_add_f32 v[172:173], v[172:173], v[142:143] op_sel:[0,1] op_sel_hi:[1,1]
	v_rcp_f32_e32 v214, v214
	v_pk_add_f32 v[174:175], v[174:175], v[142:143] op_sel:[0,1] op_sel_hi:[1,1]
	v_cvt_pk_fp8_f32 v162, v180, v181 op_sel:[0,0,1]
	v_pk_mul_f32 v[180:181], v[194:195], v[142:143] op_sel_hi:[1,0]
	v_cvt_pk_fp8_f32 v163, v160, v161
	v_pk_mul_f32 v[160:161], v[90:91], v[246:247] op_sel_hi:[1,0]
	v_exp_f32_e32 v180, v180
	v_med3_f32 v189, v189, s87, v227
	v_rcp_f32_e32 v172, v172
	v_pk_add_f32 v[156:157], v[156:157], v[142:143] op_sel:[0,1] op_sel_hi:[1,1]
	v_rcp_f32_e32 v174, v174
	v_pk_mul_f32 v[160:161], v[160:161], v[192:193]
	v_exp_f32_e32 v183, v183
	v_pk_mul_f32 v[192:193], v[46:47], v[248:249] op_sel:[0,1] op_sel_hi:[1,1]
	v_pk_mul_f32 v[160:161], v[160:161], v[196:197]
	v_pk_mul_f32 v[196:197], v[92:93], v[246:247] op_sel_hi:[1,0]
	v_cvt_pk_fp8_f32 v163, v188, v189 op_sel:[0,0,1]
	v_pk_mul_f32 v[160:161], v[160:161], v[144:145] op_sel_hi:[1,0]
	v_pk_mul_f32 v[188:189], v[82:83], v[246:247] op_sel_hi:[1,0]
	v_rcp_f32_e32 v156, v156
	v_med3_f32 v160, v160, s87, v227
	v_exp_f32_e32 v211, v211
	v_pk_mul_f32 v[196:197], v[196:197], v[198:199]
	v_exp_f32_e32 v191, v191
	v_pk_mul_f32 v[198:199], v[192:193], v[142:143] op_sel_hi:[1,0]
	v_pk_mul_f32 v[196:197], v[196:197], v[202:203]
	v_pk_mul_f32 v[202:203], v[48:49], v[248:249] op_sel:[0,1] op_sel_hi:[1,1]
	v_pk_mul_f32 v[188:189], v[188:189], v[200:201]
	v_pk_mul_f32 v[200:201], v[38:39], v[248:249] op_sel:[0,1] op_sel_hi:[1,1]
	v_pk_mul_f32 v[196:197], v[196:197], v[144:145] op_sel_hi:[1,0]
	v_pk_mul_f32 v[188:189], v[188:189], v[204:205]
	v_pk_mul_f32 v[204:205], v[84:85], v[246:247] op_sel_hi:[1,0]
	v_rcp_f32_e32 v215, v215
	v_pk_mul_f32 v[188:189], v[188:189], v[144:145] op_sel_hi:[1,0]
	v_exp_f32_e32 v181, v181
	v_med3_f32 v161, v161, s87, v227
	v_exp_f32_e32 v198, v198
	v_med3_f32 v196, v196, s87, v227
	v_med3_f32 v188, v188, s87, v227
	v_pk_mul_f32 v[204:205], v[204:205], v[206:207]
	v_pk_mul_f32 v[206:207], v[202:203], v[142:143] op_sel_hi:[1,0]
	v_rcp_f32_e32 v173, v173
	v_pk_mul_f32 v[204:205], v[204:205], v[208:209]
	v_pk_mul_f32 v[208:209], v[200:201], v[142:143] op_sel_hi:[1,0]
	v_rcp_f32_e32 v175, v175
	v_pk_mul_f32 v[204:205], v[204:205], v[144:145] op_sel_hi:[1,0]
	v_pk_add_f32 v[182:183], v[182:183], v[142:143] op_sel:[0,1] op_sel_hi:[1,1]
	v_exp_f32_e32 v206, v206
	v_cvt_pk_fp8_f32 v160, v160, v161
	v_exp_f32_e32 v208, v208
	v_med3_f32 v197, v197, s87, v227
	v_med3_f32 v189, v189, s87, v227
	v_med3_f32 v204, v204, s87, v227
	v_rcp_f32_e32 v157, v157
	v_pk_add_f32 v[210:211], v[210:211], v[142:143] op_sel:[0,1] op_sel_hi:[1,1]
	v_rcp_f32_e32 v182, v182
	v_pk_add_f32 v[190:191], v[190:191], v[142:143] op_sel:[0,1] op_sel_hi:[1,1]
	v_cvt_pk_fp8_f32 v160, v196, v197 op_sel:[0,0,1]
	v_pk_mul_f32 v[196:197], v[40:41], v[248:249] op_sel:[0,1] op_sel_hi:[1,1]
	v_cvt_pk_fp8_f32 v161, v188, v189
	v_pk_mul_f32 v[188:189], v[74:75], v[246:247] op_sel:[0,1] op_sel_hi:[1,1]
	v_med3_f32 v205, v205, s87, v227
	v_rcp_f32_e32 v210, v210
	v_pk_add_f32 v[180:181], v[180:181], v[142:143] op_sel:[0,1] op_sel_hi:[1,1]
	v_rcp_f32_e32 v190, v190
	v_pk_mul_f32 v[188:189], v[188:189], v[212:213]
	v_pk_mul_f32 v[212:213], v[196:197], v[142:143] op_sel_hi:[1,0]
	v_exp_f32_e32 v199, v199
	v_pk_mul_f32 v[188:189], v[188:189], v[214:215]
	v_exp_f32_e32 v212, v212
	v_pk_mul_f32 v[214:215], v[30:31], v[250:251] op_sel_hi:[1,0]
	v_pk_mul_f32 v[188:189], v[188:189], v[144:145] op_sel_hi:[1,0]
	v_cvt_pk_fp8_f32 v161, v204, v205 op_sel:[0,0,1]
	v_pk_mul_f32 v[204:205], v[76:77], v[246:247] op_sel:[0,1] op_sel_hi:[1,1]
	v_rcp_f32_e32 v180, v180
	v_med3_f32 v188, v188, s87, v227
	v_exp_f32_e32 v207, v207
	v_pk_mul_f32 v[204:205], v[204:205], v[158:159]
	v_pk_mul_f32 v[158:159], v[66:67], v[246:247] op_sel:[0,1] op_sel_hi:[1,1]
	v_exp_f32_e32 v209, v209
	v_pk_mul_f32 v[204:205], v[204:205], v[172:173]
	v_pk_mul_f32 v[172:173], v[214:215], v[142:143] op_sel_hi:[1,0]
	v_pk_mul_f32 v[158:159], v[158:159], v[170:171]
	v_pk_mul_f32 v[170:171], v[32:33], v[250:251] op_sel_hi:[1,0]
	v_pk_mul_f32 v[204:205], v[204:205], v[144:145] op_sel_hi:[1,0]
	v_pk_mul_f32 v[158:159], v[158:159], v[174:175]
	v_pk_mul_f32 v[174:175], v[22:23], v[250:251] op_sel_hi:[1,0]
	v_rcp_f32_e32 v183, v183
	v_pk_mul_f32 v[158:159], v[158:159], v[144:145] op_sel_hi:[1,0]
	v_exp_f32_e32 v213, v213
	v_med3_f32 v189, v189, s87, v227
	v_exp_f32_e32 v172, v172
	v_med3_f32 v204, v204, s87, v227
	v_med3_f32 v158, v158, s87, v227
	v_rcp_f32_e32 v211, v211
	v_pk_add_f32 v[198:199], v[198:199], v[142:143] op_sel:[0,1] op_sel_hi:[1,1]
	v_rcp_f32_e32 v191, v191
	v_cvt_pk_fp8_f32 v188, v188, v189
	v_med3_f32 v205, v205, s87, v227
	v_med3_f32 v159, v159, s87, v227
	v_rcp_f32_e32 v181, v181
	v_pk_add_f32 v[206:207], v[206:207], v[142:143] op_sel:[0,1] op_sel_hi:[1,1]
	v_rcp_f32_e32 v198, v198
	v_pk_add_f32 v[208:209], v[208:209], v[142:143] op_sel:[0,1] op_sel_hi:[1,1]
	v_cvt_pk_fp8_f32 v188, v204, v205 op_sel:[0,0,1]
	v_pk_mul_f32 v[204:205], v[68:69], v[246:247] op_sel:[0,1] op_sel_hi:[1,1]
	v_cvt_pk_fp8_f32 v189, v158, v159
	v_pk_mul_f32 v[158:159], v[170:171], v[142:143] op_sel_hi:[1,0]
	v_pk_mul_f32 v[204:205], v[204:205], v[178:179]
	v_pk_mul_f32 v[178:179], v[174:175], v[142:143] op_sel_hi:[1,0]
	v_exp_f32_e32 v158, v158
	v_pk_mul_f32 v[204:205], v[204:205], v[156:157]
	v_pk_mul_f32 v[156:157], v[24:25], v[250:251] op_sel_hi:[1,0]
	v_exp_f32_e32 v178, v178
	v_pk_mul_f32 v[204:205], v[204:205], v[144:145] op_sel_hi:[1,0]
	v_rcp_f32_e32 v206, v206
	v_pk_add_f32 v[212:213], v[212:213], v[142:143] op_sel:[0,1] op_sel_hi:[1,1]
	v_med3_f32 v204, v204, s87, v227
	v_rcp_f32_e32 v208, v208
	v_exp_f32_e32 v173, v173
	v_med3_f32 v205, v205, s87, v227
	v_rcp_f32_e32 v212, v212
	v_exp_f32_e32 v159, v159
	v_cvt_pk_fp8_f32 v189, v204, v205 op_sel:[0,0,1]
	v_add_u32_e32 v204, 0xe000, v219
	v_exp_f32_e32 v179, v179
	v_add_u32_e32 v205, 0x1c000, v219
	global_store_dwordx2 v204, v[162:163], s[26:27]
	v_pk_mul_f32 v[162:163], v[156:157], v[142:143] op_sel_hi:[1,0]
	global_store_dwordx2 v205, v[160:161], s[26:27]
	v_pk_mul_f32 v[160:161], v[58:59], v[248:249] op_sel_hi:[1,0]
	v_exp_f32_e32 v162, v162
	v_pk_mul_f32 v[204:205], v[14:15], v[250:251] op_sel:[0,1] op_sel_hi:[1,1]
	v_pk_mul_f32 v[160:161], v[160:161], v[176:177]
	v_pk_mul_f32 v[176:177], v[60:61], v[248:249] op_sel_hi:[1,0]
	v_rcp_f32_e32 v199, v199
	v_pk_mul_f32 v[160:161], v[160:161], v[182:183]
	v_pk_mul_f32 v[182:183], v[50:51], v[248:249] op_sel_hi:[1,0]
	v_pk_mul_f32 v[176:177], v[176:177], v[186:187]
	v_pk_mul_f32 v[160:161], v[160:161], v[144:145] op_sel_hi:[1,0]
	v_pk_mul_f32 v[186:187], v[204:205], v[142:143] op_sel_hi:[1,0]
	v_pk_mul_f32 v[176:177], v[176:177], v[210:211]
	v_pk_mul_f32 v[210:211], v[16:17], v[250:251] op_sel:[0,1] op_sel_hi:[1,1]
	v_med3_f32 v160, v160, s87, v227
	v_pk_mul_f32 v[176:177], v[176:177], v[144:145] op_sel_hi:[1,0]
	v_pk_mul_f32 v[182:183], v[182:183], v[184:185]
	v_pk_mul_f32 v[184:185], v[6:7], v[250:251] op_sel:[0,1] op_sel_hi:[1,1]
	v_exp_f32_e32 v163, v163
	v_pk_mul_f32 v[182:183], v[182:183], v[190:191]
	v_pk_mul_f32 v[190:191], v[52:53], v[248:249] op_sel_hi:[1,0]
	v_exp_f32_e32 v186, v186
	v_pk_mul_f32 v[182:183], v[182:183], v[144:145] op_sel_hi:[1,0]
	v_med3_f32 v161, v161, s87, v227
	v_med3_f32 v176, v176, s87, v227
	v_med3_f32 v182, v182, s87, v227
	v_pk_mul_f32 v[190:191], v[190:191], v[194:195]
	v_pk_mul_f32 v[194:195], v[210:211], v[142:143] op_sel_hi:[1,0]
	v_rcp_f32_e32 v207, v207
	v_pk_mul_f32 v[190:191], v[190:191], v[180:181]
	v_pk_mul_f32 v[180:181], v[184:185], v[142:143] op_sel_hi:[1,0]
	v_rcp_f32_e32 v209, v209
	v_pk_mul_f32 v[190:191], v[190:191], v[144:145] op_sel_hi:[1,0]
	v_pk_add_f32 v[172:173], v[172:173], v[142:143] op_sel:[0,1] op_sel_hi:[1,1]
	v_exp_f32_e32 v194, v194
	v_cvt_pk_fp8_f32 v160, v160, v161
	v_exp_f32_e32 v180, v180
	v_med3_f32 v177, v177, s87, v227
	v_med3_f32 v183, v183, s87, v227
	v_med3_f32 v190, v190, s87, v227
	v_rcp_f32_e32 v213, v213
	v_pk_add_f32 v[158:159], v[158:159], v[142:143] op_sel:[0,1] op_sel_hi:[1,1]
	v_rcp_f32_e32 v172, v172
	v_pk_add_f32 v[178:179], v[178:179], v[142:143] op_sel:[0,1] op_sel_hi:[1,1]
	v_cvt_pk_fp8_f32 v160, v176, v177 op_sel:[0,0,1]
	v_pk_mul_f32 v[176:177], v[8:9], v[250:251] op_sel:[0,1] op_sel_hi:[1,1]
	v_cvt_pk_fp8_f32 v161, v182, v183
	v_pk_mul_f32 v[182:183], v[42:43], v[248:249] op_sel:[0,1] op_sel_hi:[1,1]
	v_med3_f32 v191, v191, s87, v227
	v_rcp_f32_e32 v158, v158
	v_pk_add_f32 v[162:163], v[162:163], v[142:143] op_sel:[0,1] op_sel_hi:[1,1]
	v_rcp_f32_e32 v178, v178
	v_pk_mul_f32 v[182:183], v[182:183], v[192:193]
	v_pk_mul_f32 v[192:193], v[176:177], v[142:143] op_sel_hi:[1,0]
	v_exp_f32_e32 v187, v187
	v_pk_mul_f32 v[182:183], v[182:183], v[198:199]
	v_exp_f32_e32 v192, v192
	v_pk_mul_f32 v[198:199], v[44:45], v[248:249] op_sel:[0,1] op_sel_hi:[1,1]
	v_pk_mul_f32 v[182:183], v[182:183], v[144:145] op_sel_hi:[1,0]
	v_cvt_pk_fp8_f32 v161, v190, v191 op_sel:[0,0,1]
	v_pk_mul_f32 v[190:191], v[34:35], v[248:249] op_sel:[0,1] op_sel_hi:[1,1]
	v_rcp_f32_e32 v162, v162
	v_med3_f32 v182, v182, s87, v227
	v_exp_f32_e32 v195, v195
	v_pk_mul_f32 v[198:199], v[198:199], v[202:203]
	v_exp_f32_e32 v181, v181
	v_pk_mul_f32 v[190:191], v[190:191], v[200:201]
	v_pk_mul_f32 v[198:199], v[198:199], v[206:207]
	v_pk_mul_f32 v[200:201], v[36:37], v[248:249] op_sel:[0,1] op_sel_hi:[1,1]
	v_pk_mul_f32 v[190:191], v[190:191], v[208:209]
	v_pk_mul_f32 v[198:199], v[198:199], v[144:145] op_sel_hi:[1,0]
	v_rcp_f32_e32 v173, v173
	v_pk_mul_f32 v[190:191], v[190:191], v[144:145] op_sel_hi:[1,0]
	v_exp_f32_e32 v193, v193
	v_med3_f32 v183, v183, s87, v227
	v_med3_f32 v198, v198, s87, v227
	v_med3_f32 v190, v190, s87, v227
	v_pk_mul_f32 v[200:201], v[200:201], v[196:197]
	v_rcp_f32_e32 v159, v159
	v_pk_add_f32 v[186:187], v[186:187], v[142:143] op_sel:[0,1] op_sel_hi:[1,1]
	v_pk_mul_f32 v[200:201], v[200:201], v[212:213]
	v_rcp_f32_e32 v179, v179
	v_add_u32_e32 v196, 0x2a000, v219
	v_pk_mul_f32 v[200:201], v[200:201], v[144:145] op_sel_hi:[1,0]
	v_cvt_pk_fp8_f32 v182, v182, v183
	global_store_dwordx2 v196, v[188:189], s[26:27]
	v_med3_f32 v199, v199, s87, v227
	v_med3_f32 v191, v191, s87, v227
	v_med3_f32 v200, v200, s87, v227
	v_rcp_f32_e32 v163, v163
	v_pk_add_f32 v[194:195], v[194:195], v[142:143] op_sel:[0,1] op_sel_hi:[1,1]
	v_rcp_f32_e32 v186, v186
	v_pk_add_f32 v[180:181], v[180:181], v[142:143] op_sel:[0,1] op_sel_hi:[1,1]
	v_pk_mul_f32 v[188:189], v[26:27], v[250:251] op_sel_hi:[1,0]
	v_cvt_pk_fp8_f32 v182, v198, v199 op_sel:[0,0,1]
	v_cvt_pk_fp8_f32 v183, v190, v191
	v_med3_f32 v201, v201, s87, v227
	v_rcp_f32_e32 v194, v194
	v_pk_add_f32 v[192:193], v[192:193], v[142:143] op_sel:[0,1] op_sel_hi:[1,1]
	v_rcp_f32_e32 v180, v180
	v_pk_mul_f32 v[188:189], v[188:189], v[214:215]
	v_pk_mul_f32 v[190:191], v[28:29], v[250:251] op_sel_hi:[1,0]
	v_pk_mul_f32 v[196:197], v[18:19], v[250:251] op_sel_hi:[1,0]
	v_pk_mul_f32 v[188:189], v[188:189], v[172:173]
	v_cvt_pk_fp8_f32 v183, v200, v201 op_sel:[0,0,1]
	v_rcp_f32_e32 v192, v192
	v_pk_mul_f32 v[188:189], v[188:189], v[144:145] op_sel_hi:[1,0]
	v_pk_mul_f32 v[190:191], v[190:191], v[170:171]
	v_pk_mul_f32 v[196:197], v[196:197], v[174:175]
	v_med3_f32 v188, v188, s87, v227
	v_pk_mul_f32 v[190:191], v[190:191], v[158:159]
	v_pk_mul_f32 v[196:197], v[196:197], v[178:179]
	v_pk_mul_f32 v[158:159], v[20:21], v[250:251] op_sel_hi:[1,0]
	v_pk_mul_f32 v[190:191], v[190:191], v[144:145] op_sel_hi:[1,0]
	v_pk_mul_f32 v[196:197], v[196:197], v[144:145] op_sel_hi:[1,0]
	v_rcp_f32_e32 v187, v187
	v_med3_f32 v189, v189, s87, v227
	v_med3_f32 v190, v190, s87, v227
	v_med3_f32 v196, v196, s87, v227
	v_pk_mul_f32 v[158:159], v[158:159], v[156:157]
	v_rcp_f32_e32 v195, v195
	v_add_u32_e32 v156, 0x70000, v219
	v_pk_mul_f32 v[158:159], v[158:159], v[162:163]
	v_rcp_f32_e32 v181, v181
	global_store_dwordx2 v156, v[160:161], s[26:27]
	v_pk_mul_f32 v[158:159], v[158:159], v[144:145] op_sel_hi:[1,0]
	v_cvt_pk_fp8_f32 v156, v188, v189
	v_med3_f32 v191, v191, s87, v227
	v_med3_f32 v197, v197, s87, v227
	v_med3_f32 v158, v158, s87, v227
	v_rcp_f32_e32 v193, v193
	v_pk_mul_f32 v[160:161], v[10:11], v[250:251] op_sel:[0,1] op_sel_hi:[1,1]
	v_cvt_pk_fp8_f32 v156, v190, v191 op_sel:[0,0,1]
	v_cvt_pk_fp8_f32 v157, v196, v197
	v_med3_f32 v159, v159, s87, v227
	v_pk_mul_f32 v[160:161], v[160:161], v[204:205]
	v_pk_mul_f32 v[162:163], v[12:13], v[250:251] op_sel:[0,1] op_sel_hi:[1,1]
	v_pk_mul_f32 v[170:171], v[2:3], v[250:251] op_sel:[0,1] op_sel_hi:[1,1]
	v_pk_mul_f32 v[160:161], v[160:161], v[186:187]
	v_cvt_pk_fp8_f32 v157, v158, v159 op_sel:[0,0,1]
	v_pk_mul_f32 v[162:163], v[162:163], v[210:211]
	v_pk_mul_f32 v[160:161], v[160:161], v[144:145] op_sel_hi:[1,0]
	v_pk_mul_f32 v[170:171], v[170:171], v[184:185]
	v_pk_mul_f32 v[162:163], v[162:163], v[194:195]
	v_med3_f32 v160, v160, s87, v227
	v_pk_mul_f32 v[170:171], v[170:171], v[180:181]
	v_pk_mul_f32 v[162:163], v[162:163], v[144:145] op_sel_hi:[1,0]
	v_pk_mul_f32 v[158:159], v[4:5], v[250:251] op_sel:[0,1] op_sel_hi:[1,1]
	v_pk_mul_f32 v[170:171], v[170:171], v[144:145] op_sel_hi:[1,0]
	v_med3_f32 v161, v161, s87, v227
	v_med3_f32 v162, v162, s87, v227
	v_med3_f32 v170, v170, s87, v227
	v_pk_mul_f32 v[158:159], v[158:159], v[176:177]
	v_add_u32_e32 v172, 0x7e000, v219
	v_cvt_pk_fp8_f32 v160, v160, v161
	v_pk_mul_f32 v[158:159], v[158:159], v[192:193]
	global_store_dwordx2 v172, v[182:183], s[26:27]
	v_med3_f32 v163, v163, s87, v227
	v_pk_mul_f32 v[158:159], v[158:159], v[144:145] op_sel_hi:[1,0]
	v_med3_f32 v171, v171, s87, v227
	v_cvt_pk_fp8_f32 v160, v162, v163 op_sel:[0,0,1]
	v_med3_f32 v158, v158, s87, v227
	v_cvt_pk_fp8_f32 v161, v170, v171
	v_add_u32_e32 v162, 0x8c000, v219
	v_med3_f32 v159, v159, s87, v227
	v_add_u32_e32 v163, 0x9a000, v219
	global_store_dwordx2 v162, v[156:157], s[26:27]
	v_cvt_pk_fp8_f32 v161, v158, v159 op_sel:[0,0,1]
	global_store_dwordx2 v163, v[160:161], s[26:27]
	s_andn2_b64 vcc, exec, s[46:47]
	s_mov_b64 s[46:47], -1
	s_cbranch_vccnz .LBB0_807
	s_andn2_b64 vcc, exec, s[30:31]
	s_cbranch_vccnz .LBB0_806
	s_barrier
	s_branch .LBB0_806

.LBB0_840:
	s_ashr_i32 s43, s42, 31
	s_lshl_b64 s[46:47], s[42:43], 18
	s_add_u32 s46, s8, s46
	s_addc_u32 s47, s10, s47
	s_ashr_i32 s41, s40, 31
	s_lshl_b64 s[48:49], s[40:41], 18
	s_add_u32 s48, s11, s48
	s_addc_u32 s49, s12, s49
	s_andn2_b64 vcc, exec, s[34:35]
	s_cbranch_vccnz .LBB0_848
	v_lshl_add_u32 v2, s50, 8, v195
	v_ashrrev_i32_e32 v3, 31, v2
	v_lshl_add_u64 v[4:5], v[2:3], 2, v[180:181]
	global_load_dword v244, v[4:5], off
	global_load_dword v245, v[4:5], off offset:64
	global_load_dword v246, v[4:5], off offset:128
	global_load_dword v247, v[4:5], off offset:192
	global_load_dword v248, v[4:5], off offset:512
	global_load_dword v249, v[4:5], off offset:576
	global_load_dword v250, v[4:5], off offset:640
	global_load_dword v251, v[4:5], off offset:704
	s_and_b64 s[58:59], s[44:45], exec
	s_cselect_b32 s41, s47, s53
	s_cselect_b32 s43, s46, s52
	s_cselect_b32 s62, s49, s55
	s_cselect_b32 s63, s48, s54
	s_add_u32 s64, s54, 0x100
	s_addc_u32 s65, s55, 0
	s_add_u32 s52, s52, 0x20080
	v_mov_b32_e32 v66, 0
	v_mov_b32_e32 v1, 0x3ecc95a3
	s_addc_u32 s53, s53, 0
	s_mov_b32 s54, 0
	v_mov_b32_e32 v67, v66
	v_mov_b32_e32 v68, v66
	v_mov_b32_e32 v69, v66
	v_mov_b32_e32 v74, v66
	v_mov_b32_e32 v75, v66
	v_mov_b32_e32 v76, v66
	v_mov_b32_e32 v77, v66
	v_mov_b32_e32 v82, v66
	v_mov_b32_e32 v83, v66
	v_mov_b32_e32 v84, v66
	v_mov_b32_e32 v85, v66
	v_mov_b32_e32 v90, v66
	v_mov_b32_e32 v91, v66
	v_mov_b32_e32 v92, v66
	v_mov_b32_e32 v93, v66
	v_mov_b32_e32 v38, v66
	v_mov_b32_e32 v39, v66
	v_mov_b32_e32 v40, v66
	v_mov_b32_e32 v41, v66
	v_mov_b32_e32 v46, v66
	v_mov_b32_e32 v47, v66
	v_mov_b32_e32 v48, v66
	v_mov_b32_e32 v49, v66
	v_mov_b32_e32 v54, v66
	v_mov_b32_e32 v55, v66
	v_mov_b32_e32 v56, v66
	v_mov_b32_e32 v57, v66
	v_mov_b32_e32 v62, v66
	v_mov_b32_e32 v63, v66
	v_mov_b32_e32 v64, v66
	v_mov_b32_e32 v65, v66
	v_mov_b32_e32 v70, v66
	v_mov_b32_e32 v71, v66
	v_mov_b32_e32 v72, v66
	v_mov_b32_e32 v73, v66
	v_mov_b32_e32 v78, v66
	v_mov_b32_e32 v79, v66
	v_mov_b32_e32 v80, v66
	v_mov_b32_e32 v81, v66
	v_mov_b32_e32 v86, v66
	v_mov_b32_e32 v87, v66
	v_mov_b32_e32 v88, v66
	v_mov_b32_e32 v89, v66
	v_mov_b32_e32 v94, v66
	v_mov_b32_e32 v95, v66
	v_mov_b32_e32 v96, v66
	v_mov_b32_e32 v97, v66
	v_mov_b32_e32 v98, v66
	v_mov_b32_e32 v99, v66
	v_mov_b32_e32 v100, v66
	v_mov_b32_e32 v101, v66
	v_mov_b32_e32 v106, v66
	v_mov_b32_e32 v107, v66
	v_mov_b32_e32 v108, v66
	v_mov_b32_e32 v109, v66
	v_mov_b32_e32 v114, v66
	v_mov_b32_e32 v115, v66
	v_mov_b32_e32 v116, v66
	v_mov_b32_e32 v117, v66
	v_mov_b32_e32 v122, v66
	v_mov_b32_e32 v123, v66
	v_mov_b32_e32 v124, v66
	v_mov_b32_e32 v125, v66
	v_mov_b32_e32 v130, v66
	v_mov_b32_e32 v131, v66
	v_mov_b32_e32 v132, v66
	v_mov_b32_e32 v133, v66
	v_mov_b32_e32 v138, v66
	v_mov_b32_e32 v139, v66
	v_mov_b32_e32 v140, v66
	v_mov_b32_e32 v141, v66
	v_mov_b32_e32 v146, v66
	v_mov_b32_e32 v147, v66
	v_mov_b32_e32 v148, v66
	v_mov_b32_e32 v149, v66
	v_mov_b32_e32 v154, v66
	v_mov_b32_e32 v155, v66
	v_mov_b32_e32 v156, v66
	v_mov_b32_e32 v157, v66
	v_mov_b32_e32 v102, v66
	v_mov_b32_e32 v103, v66
	v_mov_b32_e32 v104, v66
	v_mov_b32_e32 v105, v66
	v_mov_b32_e32 v110, v66
	v_mov_b32_e32 v111, v66
	v_mov_b32_e32 v112, v66
	v_mov_b32_e32 v113, v66
	v_mov_b32_e32 v118, v66
	v_mov_b32_e32 v119, v66
	v_mov_b32_e32 v120, v66
	v_mov_b32_e32 v121, v66
	v_mov_b32_e32 v126, v66
	v_mov_b32_e32 v127, v66
	v_mov_b32_e32 v128, v66
	v_mov_b32_e32 v129, v66
	v_mov_b32_e32 v134, v66
	v_mov_b32_e32 v135, v66
	v_mov_b32_e32 v136, v66
	v_mov_b32_e32 v137, v66
	v_mov_b32_e32 v142, v66
	v_mov_b32_e32 v143, v66
	v_mov_b32_e32 v144, v66
	v_mov_b32_e32 v145, v66
	v_mov_b32_e32 v150, v66
	v_mov_b32_e32 v151, v66
	v_mov_b32_e32 v152, v66
	v_mov_b32_e32 v153, v66
	v_mov_b32_e32 v158, v66
	v_mov_b32_e32 v159, v66
	v_mov_b32_e32 v160, v66
	v_mov_b32_e32 v161, v66
	v_mov_b32_e32 v58, v66
	v_mov_b32_e32 v59, v66
	v_mov_b32_e32 v60, v66
	v_mov_b32_e32 v61, v66
	v_mov_b32_e32 v50, v66
	v_mov_b32_e32 v51, v66
	v_mov_b32_e32 v52, v66
	v_mov_b32_e32 v53, v66
	v_mov_b32_e32 v42, v66
	v_mov_b32_e32 v43, v66
	v_mov_b32_e32 v44, v66
	v_mov_b32_e32 v45, v66
	v_mov_b32_e32 v34, v66
	v_mov_b32_e32 v35, v66
	v_mov_b32_e32 v36, v66
	v_mov_b32_e32 v37, v66

.LBB0_845:
	v_xor_b32_e32 v240, 16, v231
	v_and_b32_e32 v238, 64, v231
	v_add_u32_e32 v238, 64, v238
	v_xor_b32_e32 v239, 32, v231
	v_cmp_lt_i32_e32 vcc, v240, v238
	v_mov_b32_e32 v2, 0xbfb8aa3b
	v_mov_b32_e32 v3, 1.0
	v_cndmask_b32_e32 v240, v231, v240, vcc
	v_cmp_lt_i32_e32 vcc, v239, v238
	v_lshlrev_b32_e32 v240, 2, v240
	v_mov_b32_e32 v4, 0x41000000
	v_cndmask_b32_e32 v239, v231, v239, vcc
	v_lshlrev_b32_e32 v239, 2, v239
	ds_bpermute_b32 v6, v240, v244
	ds_bpermute_b32 v7, v240, v245
	ds_bpermute_b32 v8, v240, v246
	ds_bpermute_b32 v9, v240, v247
	ds_bpermute_b32 v10, v240, v248
	ds_bpermute_b32 v11, v240, v249
	ds_bpermute_b32 v12, v240, v250
	ds_bpermute_b32 v13, v240, v251
	v_lshl_add_u32 v243, s50, 8, v195
	v_lshl_or_b32 v242, s61, 7, v197
	v_mad_u32_u24 v241, v243, s33, v242
	s_waitcnt lgkmcnt(7)
	v_add_f32_e32 v244, v244, v6
	ds_bpermute_b32 v6, v239, v244
	s_waitcnt lgkmcnt(7)
	v_add_f32_e32 v245, v245, v7
	ds_bpermute_b32 v7, v239, v245
	s_waitcnt lgkmcnt(7)
	v_add_f32_e32 v246, v246, v8
	ds_bpermute_b32 v8, v239, v246
	s_waitcnt lgkmcnt(7)
	v_add_f32_e32 v247, v247, v9
	ds_bpermute_b32 v9, v239, v247
	s_waitcnt lgkmcnt(7)
	v_add_f32_e32 v248, v248, v10
	ds_bpermute_b32 v10, v239, v248
	s_waitcnt lgkmcnt(7)
	v_add_f32_e32 v249, v249, v11
	ds_bpermute_b32 v11, v239, v249
	s_waitcnt lgkmcnt(7)
	v_add_f32_e32 v250, v250, v12
	ds_bpermute_b32 v12, v239, v250
	s_waitcnt lgkmcnt(7)
	v_add_f32_e32 v251, v251, v13
	ds_bpermute_b32 v13, v239, v251
	s_waitcnt lgkmcnt(7)
	v_add_f32_e32 v244, v244, v6
	v_fmamk_f32 v244, v244, 0x3a800000, v224
	s_waitcnt lgkmcnt(6)
	v_add_f32_e32 v245, v245, v7
	v_fmamk_f32 v245, v245, 0x3a800000, v224
	s_waitcnt lgkmcnt(5)
	v_add_f32_e32 v246, v246, v8
	v_fmamk_f32 v246, v246, 0x3a800000, v224
	s_waitcnt lgkmcnt(4)
	v_add_f32_e32 v247, v247, v9
	v_fmamk_f32 v247, v247, 0x3a800000, v224
	s_waitcnt lgkmcnt(3)
	v_add_f32_e32 v248, v248, v10
	v_fmamk_f32 v248, v248, 0x3a800000, v224
	s_waitcnt lgkmcnt(2)
	v_add_f32_e32 v249, v249, v11
	v_fmamk_f32 v249, v249, 0x3a800000, v224
	s_waitcnt lgkmcnt(1)
	v_add_f32_e32 v250, v250, v12
	v_fmamk_f32 v250, v250, 0x3a800000, v224
	s_waitcnt lgkmcnt(0)
	v_add_f32_e32 v251, v251, v13
	v_fmamk_f32 v251, v251, 0x3a800000, v224
	v_rsq_f32_e32 v244, v244
	v_rsq_f32_e32 v245, v245
	v_rsq_f32_e32 v246, v246
	v_rsq_f32_e32 v247, v247
	v_rsq_f32_e32 v248, v248
	v_rsq_f32_e32 v249, v249
	v_rsq_f32_e32 v250, v250
	v_rsq_f32_e32 v251, v251
	v_pk_mul_f32 v[6:7], v[158:159], v[244:245] op_sel_hi:[1,0]
	v_pk_mul_f32 v[8:9], v[160:161], v[244:245] op_sel_hi:[1,0]
	v_pk_mul_f32 v[10:11], v[150:151], v[244:245] op_sel_hi:[1,0]
	v_pk_mul_f32 v[12:13], v[6:7], v[2:3] op_sel_hi:[1,0]
	v_pk_mul_f32 v[14:15], v[8:9], v[2:3] op_sel_hi:[1,0]
	v_pk_mul_f32 v[16:17], v[10:11], v[2:3] op_sel_hi:[1,0]
	v_exp_f32_e32 v12, v12
	v_pk_mul_f32 v[18:19], v[152:153], v[244:245] op_sel_hi:[1,0]
	v_exp_f32_e32 v14, v14
	v_pk_mul_f32 v[20:21], v[142:143], v[244:245] op_sel:[0,1] op_sel_hi:[1,1]
	v_exp_f32_e32 v16, v16
	v_pk_mul_f32 v[22:23], v[18:19], v[2:3] op_sel_hi:[1,0]
	v_pk_mul_f32 v[24:25], v[20:21], v[2:3] op_sel_hi:[1,0]
	v_pk_mul_f32 v[26:27], v[144:145], v[244:245] op_sel:[0,1] op_sel_hi:[1,1]
	v_exp_f32_e32 v22, v22
	v_pk_mul_f32 v[28:29], v[134:135], v[244:245] op_sel:[0,1] op_sel_hi:[1,1]
	v_exp_f32_e32 v13, v13
	v_pk_mul_f32 v[30:31], v[26:27], v[2:3] op_sel_hi:[1,0]
	v_exp_f32_e32 v15, v15
	v_pk_mul_f32 v[32:33], v[28:29], v[2:3] op_sel_hi:[1,0]
	v_exp_f32_e32 v17, v17
	v_pk_mul_f32 v[186:187], v[136:137], v[244:245] op_sel:[0,1] op_sel_hi:[1,1]
	v_exp_f32_e32 v23, v23
	v_pk_mul_f32 v[188:189], v[126:127], v[246:247] op_sel_hi:[1,0]
	v_exp_f32_e32 v24, v24
	v_pk_add_f32 v[12:13], v[12:13], v[2:3] op_sel:[0,1] op_sel_hi:[1,1]
	v_exp_f32_e32 v30, v30
	v_pk_mul_f32 v[190:191], v[186:187], v[2:3] op_sel_hi:[1,0]
	v_exp_f32_e32 v32, v32
	v_pk_add_f32 v[14:15], v[14:15], v[2:3] op_sel:[0,1] op_sel_hi:[1,1]
	v_rcp_f32_e32 v12, v12
	v_pk_add_f32 v[16:17], v[16:17], v[2:3] op_sel:[0,1] op_sel_hi:[1,1]
	v_exp_f32_e32 v190, v190
	v_pk_add_f32 v[22:23], v[22:23], v[2:3] op_sel:[0,1] op_sel_hi:[1,1]
	v_rcp_f32_e32 v14, v14
	v_pk_mul_f32 v[192:193], v[188:189], v[2:3] op_sel_hi:[1,0]
	v_rcp_f32_e32 v16, v16
	v_pk_mul_f32 v[200:201], v[128:129], v[246:247] op_sel_hi:[1,0]
	v_exp_f32_e32 v25, v25
	v_pk_mul_f32 v[202:203], v[118:119], v[246:247] op_sel_hi:[1,0]
	v_rcp_f32_e32 v22, v22
	v_pk_mul_f32 v[204:205], v[200:201], v[2:3] op_sel_hi:[1,0]
	v_exp_f32_e32 v31, v31
	v_pk_mul_f32 v[206:207], v[202:203], v[2:3] op_sel_hi:[1,0]
	v_exp_f32_e32 v33, v33
	v_pk_mul_f32 v[208:209], v[120:121], v[246:247] op_sel_hi:[1,0]
	v_rcp_f32_e32 v13, v13
	v_pk_add_f32 v[24:25], v[24:25], v[2:3] op_sel:[0,1] op_sel_hi:[1,1]
	v_exp_f32_e32 v191, v191
	v_pk_mul_f32 v[210:211], v[208:209], v[2:3] op_sel_hi:[1,0]
	v_exp_f32_e32 v192, v192
	v_pk_add_f32 v[30:31], v[30:31], v[2:3] op_sel:[0,1] op_sel_hi:[1,1]
	v_rcp_f32_e32 v15, v15
	v_pk_add_f32 v[32:33], v[32:33], v[2:3] op_sel:[0,1] op_sel_hi:[1,1]
	v_rcp_f32_e32 v17, v17
	v_pk_mul_f32 v[212:213], v[154:155], v[244:245] op_sel_hi:[1,0]
	v_exp_f32_e32 v204, v204
	v_pk_add_f32 v[190:191], v[190:191], v[2:3] op_sel:[0,1] op_sel_hi:[1,1]
	v_exp_f32_e32 v206, v206
	v_pk_mul_f32 v[214:215], v[110:111], v[246:247] op_sel:[0,1] op_sel_hi:[1,1]
	v_rcp_f32_e32 v23, v23
	v_pk_mul_f32 v[212:213], v[212:213], v[6:7]
	v_rcp_f32_e32 v24, v24
	v_pk_mul_f32 v[6:7], v[156:157], v[244:245] op_sel_hi:[1,0]
	v_exp_f32_e32 v210, v210
	v_pk_mul_f32 v[212:213], v[212:213], v[12:13]
	v_rcp_f32_e32 v30, v30
	v_pk_mul_f32 v[12:13], v[146:147], v[244:245] op_sel_hi:[1,0]
	v_rcp_f32_e32 v32, v32
	v_pk_mul_f32 v[212:213], v[212:213], v[4:5] op_sel_hi:[1,0]
	v_exp_f32_e32 v193, v193
	v_pk_mul_f32 v[216:217], v[214:215], v[2:3] op_sel_hi:[1,0]
	v_rcp_f32_e32 v190, v190
	v_pk_mul_f32 v[218:219], v[112:113], v[246:247] op_sel:[0,1] op_sel_hi:[1,1]
	v_exp_f32_e32 v205, v205
	v_pk_mul_f32 v[220:221], v[102:103], v[246:247] op_sel:[0,1] op_sel_hi:[1,1]
	v_exp_f32_e32 v207, v207
	v_med3_f32 v212, v212, s87, v227
	v_pk_mul_f32 v[6:7], v[6:7], v[8:9]
	v_pk_mul_f32 v[12:13], v[12:13], v[10:11]
	v_pk_mul_f32 v[8:9], v[148:149], v[244:245] op_sel_hi:[1,0]
	v_pk_mul_f32 v[6:7], v[6:7], v[14:15]
	v_pk_mul_f32 v[12:13], v[12:13], v[16:17]
	v_rcp_f32_e32 v25, v25
	v_pk_mul_f32 v[6:7], v[6:7], v[4:5] op_sel_hi:[1,0]
	v_pk_mul_f32 v[12:13], v[12:13], v[4:5] op_sel_hi:[1,0]
	v_exp_f32_e32 v211, v211
	v_pk_mul_f32 v[10:11], v[218:219], v[2:3] op_sel_hi:[1,0]
	v_exp_f32_e32 v216, v216
	v_pk_mul_f32 v[14:15], v[220:221], v[2:3] op_sel_hi:[1,0]
	v_pk_mul_f32 v[16:17], v[104:105], v[246:247] op_sel:[0,1] op_sel_hi:[1,1]
	v_med3_f32 v213, v213, s87, v227
	v_med3_f32 v6, v6, s87, v227
	v_med3_f32 v12, v12, s87, v227
	v_pk_mul_f32 v[8:9], v[8:9], v[18:19]
	v_rcp_f32_e32 v31, v31
	v_pk_add_f32 v[192:193], v[192:193], v[2:3] op_sel:[0,1] op_sel_hi:[1,1]
	v_pk_mul_f32 v[8:9], v[8:9], v[22:23]
	v_rcp_f32_e32 v33, v33
	v_pk_mul_f32 v[18:19], v[16:17], v[2:3] op_sel_hi:[1,0]
	v_pk_mul_f32 v[8:9], v[8:9], v[4:5] op_sel_hi:[1,0]
	v_exp_f32_e32 v10, v10
	v_cvt_pk_fp8_f32 v22, v212, v213
	v_exp_f32_e32 v14, v14
	v_med3_f32 v7, v7, s87, v227
	v_med3_f32 v13, v13, s87, v227
	v_med3_f32 v8, v8, s87, v227
	v_rcp_f32_e32 v191, v191
	v_pk_add_f32 v[204:205], v[204:205], v[2:3] op_sel:[0,1] op_sel_hi:[1,1]
	v_rcp_f32_e32 v192, v192
	v_pk_add_f32 v[206:207], v[206:207], v[2:3] op_sel:[0,1] op_sel_hi:[1,1]
	v_exp_f32_e32 v18, v18
	v_pk_mul_f32 v[212:213], v[138:139], v[244:245] op_sel:[0,1] op_sel_hi:[1,1]
	v_cvt_pk_fp8_f32 v22, v6, v7 op_sel:[0,0,1]
	v_cvt_pk_fp8_f32 v23, v12, v13
	v_med3_f32 v9, v9, s87, v227
	v_rcp_f32_e32 v204, v204
	v_pk_add_f32 v[210:211], v[210:211], v[2:3] op_sel:[0,1] op_sel_hi:[1,1]
	v_rcp_f32_e32 v206, v206
	v_pk_mul_f32 v[6:7], v[94:95], v[248:249] op_sel_hi:[1,0]
	v_exp_f32_e32 v217, v217
	v_pk_mul_f32 v[212:213], v[212:213], v[20:21]
	v_pk_mul_f32 v[12:13], v[140:141], v[244:245] op_sel:[0,1] op_sel_hi:[1,1]
	v_pk_mul_f32 v[20:21], v[130:131], v[244:245] op_sel:[0,1] op_sel_hi:[1,1]
	v_pk_mul_f32 v[212:213], v[212:213], v[24:25]
	v_cvt_pk_fp8_f32 v23, v8, v9 op_sel:[0,0,1]
	v_rcp_f32_e32 v210, v210
	v_pk_mul_f32 v[212:213], v[212:213], v[4:5] op_sel_hi:[1,0]
	v_exp_f32_e32 v11, v11
	v_pk_mul_f32 v[8:9], v[6:7], v[2:3] op_sel_hi:[1,0]
	v_exp_f32_e32 v15, v15
	v_pk_mul_f32 v[24:25], v[96:97], v[248:249] op_sel_hi:[1,0]
	v_pk_mul_f32 v[222:223], v[86:87], v[248:249] op_sel_hi:[1,0]
	v_med3_f32 v212, v212, s87, v227
	v_pk_mul_f32 v[12:13], v[12:13], v[26:27]
	v_pk_mul_f32 v[20:21], v[20:21], v[28:29]
	v_pk_mul_f32 v[26:27], v[132:133], v[244:245] op_sel:[0,1] op_sel_hi:[1,1]
	v_pk_mul_f32 v[12:13], v[12:13], v[30:31]
	v_pk_mul_f32 v[20:21], v[20:21], v[32:33]
	v_rcp_f32_e32 v193, v193
	v_pk_mul_f32 v[12:13], v[12:13], v[4:5] op_sel_hi:[1,0]
	v_pk_mul_f32 v[20:21], v[20:21], v[4:5] op_sel_hi:[1,0]
	global_store_dwordx2 v241, v[22:23], s[26:27]
	v_exp_f32_e32 v19, v19
	v_pk_mul_f32 v[22:23], v[24:25], v[2:3] op_sel_hi:[1,0]
	v_exp_f32_e32 v8, v8
	v_pk_mul_f32 v[28:29], v[222:223], v[2:3] op_sel_hi:[1,0]
	v_pk_mul_f32 v[30:31], v[88:89], v[248:249] op_sel_hi:[1,0]
	v_med3_f32 v213, v213, s87, v227
	v_med3_f32 v12, v12, s87, v227
	v_med3_f32 v20, v20, s87, v227
	v_pk_mul_f32 v[26:27], v[26:27], v[186:187]
	v_rcp_f32_e32 v205, v205
	v_pk_add_f32 v[216:217], v[216:217], v[2:3] op_sel:[0,1] op_sel_hi:[1,1]
	v_pk_mul_f32 v[26:27], v[26:27], v[190:191]
	v_rcp_f32_e32 v207, v207
	v_pk_mul_f32 v[32:33], v[30:31], v[2:3] op_sel_hi:[1,0]
	v_pk_mul_f32 v[26:27], v[26:27], v[4:5] op_sel_hi:[1,0]
	v_exp_f32_e32 v22, v22
	v_cvt_pk_fp8_f32 v186, v212, v213
	v_exp_f32_e32 v28, v28
	v_med3_f32 v13, v13, s87, v227
	v_med3_f32 v21, v21, s87, v227
	v_med3_f32 v26, v26, s87, v227
	v_rcp_f32_e32 v211, v211
	v_pk_add_f32 v[10:11], v[10:11], v[2:3] op_sel:[0,1] op_sel_hi:[1,1]
	v_rcp_f32_e32 v216, v216
	v_pk_add_f32 v[14:15], v[14:15], v[2:3] op_sel:[0,1] op_sel_hi:[1,1]
	v_exp_f32_e32 v32, v32
	v_pk_mul_f32 v[190:191], v[122:123], v[246:247] op_sel_hi:[1,0]
	v_cvt_pk_fp8_f32 v186, v12, v13 op_sel:[0,0,1]
	v_cvt_pk_fp8_f32 v187, v20, v21
	v_med3_f32 v27, v27, s87, v227
	v_rcp_f32_e32 v10, v10
	v_pk_add_f32 v[18:19], v[18:19], v[2:3] op_sel:[0,1] op_sel_hi:[1,1]
	v_rcp_f32_e32 v14, v14
	v_pk_mul_f32 v[12:13], v[78:79], v[248:249] op_sel:[0,1] op_sel_hi:[1,1]
	v_exp_f32_e32 v9, v9
	v_pk_mul_f32 v[190:191], v[190:191], v[188:189]
	v_pk_mul_f32 v[20:21], v[124:125], v[246:247] op_sel_hi:[1,0]
	v_pk_mul_f32 v[188:189], v[114:115], v[246:247] op_sel_hi:[1,0]
	v_pk_mul_f32 v[190:191], v[190:191], v[192:193]
	v_cvt_pk_fp8_f32 v187, v26, v27 op_sel:[0,0,1]
	v_rcp_f32_e32 v18, v18
	v_pk_mul_f32 v[190:191], v[190:191], v[4:5] op_sel_hi:[1,0]
	v_exp_f32_e32 v23, v23
	v_pk_mul_f32 v[26:27], v[12:13], v[2:3] op_sel_hi:[1,0]
	v_exp_f32_e32 v29, v29
	v_pk_mul_f32 v[192:193], v[80:81], v[248:249] op_sel:[0,1] op_sel_hi:[1,1]
	v_pk_mul_f32 v[212:213], v[70:71], v[248:249] op_sel:[0,1] op_sel_hi:[1,1]
	v_med3_f32 v190, v190, s87, v227
	v_pk_mul_f32 v[20:21], v[20:21], v[200:201]
	v_pk_mul_f32 v[188:189], v[188:189], v[202:203]
	v_pk_mul_f32 v[200:201], v[116:117], v[246:247] op_sel_hi:[1,0]
	v_pk_mul_f32 v[20:21], v[20:21], v[204:205]
	v_pk_mul_f32 v[188:189], v[188:189], v[206:207]
	v_rcp_f32_e32 v217, v217
	v_pk_mul_f32 v[20:21], v[20:21], v[4:5] op_sel_hi:[1,0]
	v_pk_mul_f32 v[188:189], v[188:189], v[4:5] op_sel_hi:[1,0]
	v_exp_f32_e32 v33, v33
	v_pk_mul_f32 v[202:203], v[192:193], v[2:3] op_sel_hi:[1,0]
	v_exp_f32_e32 v26, v26
	v_pk_mul_f32 v[204:205], v[212:213], v[2:3] op_sel_hi:[1,0]
	v_pk_mul_f32 v[206:207], v[72:73], v[248:249] op_sel:[0,1] op_sel_hi:[1,1]
	v_med3_f32 v191, v191, s87, v227
	v_med3_f32 v20, v20, s87, v227
	v_med3_f32 v188, v188, s87, v227
	v_pk_mul_f32 v[200:201], v[200:201], v[208:209]
	v_rcp_f32_e32 v11, v11
	v_pk_add_f32 v[8:9], v[8:9], v[2:3] op_sel:[0,1] op_sel_hi:[1,1]
	v_pk_mul_f32 v[200:201], v[200:201], v[210:211]
	v_rcp_f32_e32 v15, v15
	v_pk_mul_f32 v[208:209], v[206:207], v[2:3] op_sel_hi:[1,0]
	v_pk_mul_f32 v[200:201], v[200:201], v[4:5] op_sel_hi:[1,0]
	v_exp_f32_e32 v202, v202
	v_cvt_pk_fp8_f32 v190, v190, v191
	v_exp_f32_e32 v204, v204
	v_med3_f32 v21, v21, s87, v227
	v_med3_f32 v189, v189, s87, v227
	v_med3_f32 v200, v200, s87, v227
	v_rcp_f32_e32 v19, v19
	v_pk_add_f32 v[22:23], v[22:23], v[2:3] op_sel:[0,1] op_sel_hi:[1,1]
	v_rcp_f32_e32 v8, v8
	v_pk_add_f32 v[28:29], v[28:29], v[2:3] op_sel:[0,1] op_sel_hi:[1,1]
	v_exp_f32_e32 v208, v208
	v_pk_mul_f32 v[210:211], v[106:107], v[246:247] op_sel:[0,1] op_sel_hi:[1,1]
	v_cvt_pk_fp8_f32 v190, v20, v21 op_sel:[0,0,1]
	v_cvt_pk_fp8_f32 v191, v188, v189
	v_med3_f32 v201, v201, s87, v227
	v_rcp_f32_e32 v22, v22
	v_pk_add_f32 v[32:33], v[32:33], v[2:3] op_sel:[0,1] op_sel_hi:[1,1]
	v_rcp_f32_e32 v28, v28
	v_pk_mul_f32 v[20:21], v[62:63], v[250:251] op_sel_hi:[1,0]
	v_exp_f32_e32 v27, v27
	v_pk_mul_f32 v[210:211], v[210:211], v[214:215]
	v_pk_mul_f32 v[188:189], v[108:109], v[246:247] op_sel:[0,1] op_sel_hi:[1,1]
	v_pk_mul_f32 v[214:215], v[98:99], v[246:247] op_sel:[0,1] op_sel_hi:[1,1]
	v_pk_mul_f32 v[210:211], v[210:211], v[216:217]
	v_cvt_pk_fp8_f32 v191, v200, v201 op_sel:[0,0,1]
	v_rcp_f32_e32 v32, v32
	v_pk_mul_f32 v[210:211], v[210:211], v[4:5] op_sel_hi:[1,0]
	v_exp_f32_e32 v203, v203
	v_pk_mul_f32 v[200:201], v[20:21], v[2:3] op_sel_hi:[1,0]
	v_exp_f32_e32 v205, v205
	v_pk_mul_f32 v[216:217], v[64:65], v[250:251] op_sel_hi:[1,0]
	v_pk_mul_f32 v[236:237], v[54:55], v[250:251] op_sel_hi:[1,0]
	v_med3_f32 v210, v210, s87, v227
	v_pk_mul_f32 v[188:189], v[188:189], v[218:219]
	v_pk_mul_f32 v[214:215], v[214:215], v[220:221]
	v_pk_mul_f32 v[218:219], v[100:101], v[246:247] op_sel:[0,1] op_sel_hi:[1,1]
	v_pk_mul_f32 v[188:189], v[188:189], v[10:11]
	v_pk_mul_f32 v[214:215], v[214:215], v[14:15]
	v_rcp_f32_e32 v9, v9
	v_pk_mul_f32 v[188:189], v[188:189], v[4:5] op_sel_hi:[1,0]
	v_pk_mul_f32 v[214:215], v[214:215], v[4:5] op_sel_hi:[1,0]
	v_exp_f32_e32 v209, v209
	v_pk_mul_f32 v[10:11], v[216:217], v[2:3] op_sel_hi:[1,0]
	v_exp_f32_e32 v200, v200
	v_pk_mul_f32 v[14:15], v[236:237], v[2:3] op_sel_hi:[1,0]
	v_pk_mul_f32 v[220:221], v[56:57], v[250:251] op_sel_hi:[1,0]
	v_med3_f32 v211, v211, s87, v227
	v_med3_f32 v188, v188, s87, v227
	v_med3_f32 v214, v214, s87, v227
	v_pk_mul_f32 v[218:219], v[218:219], v[16:17]
	v_rcp_f32_e32 v23, v23
	v_pk_add_f32 v[26:27], v[26:27], v[2:3] op_sel:[0,1] op_sel_hi:[1,1]
	v_pk_mul_f32 v[218:219], v[218:219], v[18:19]
	v_rcp_f32_e32 v29, v29
	v_add_u32_e32 v16, 0xe000, v241
	v_pk_mul_f32 v[218:219], v[218:219], v[4:5] op_sel_hi:[1,0]
	v_exp_f32_e32 v10, v10
	global_store_dwordx2 v16, v[186:187], s[26:27]
	v_exp_f32_e32 v14, v14
	v_pk_mul_f32 v[16:17], v[220:221], v[2:3] op_sel_hi:[1,0]
	v_cvt_pk_fp8_f32 v18, v210, v211
	v_med3_f32 v189, v189, s87, v227
	v_med3_f32 v215, v215, s87, v227
	v_med3_f32 v218, v218, s87, v227
	v_rcp_f32_e32 v33, v33
	v_pk_add_f32 v[202:203], v[202:203], v[2:3] op_sel:[0,1] op_sel_hi:[1,1]
	v_rcp_f32_e32 v26, v26
	v_pk_add_f32 v[204:205], v[204:205], v[2:3] op_sel:[0,1] op_sel_hi:[1,1]
	v_exp_f32_e32 v16, v16
	v_pk_mul_f32 v[186:187], v[90:91], v[248:249] op_sel_hi:[1,0]
	v_cvt_pk_fp8_f32 v18, v188, v189 op_sel:[0,0,1]
	v_cvt_pk_fp8_f32 v19, v214, v215
	v_med3_f32 v219, v219, s87, v227
	v_rcp_f32_e32 v202, v202
	v_pk_add_f32 v[208:209], v[208:209], v[2:3] op_sel:[0,1] op_sel_hi:[1,1]
	v_rcp_f32_e32 v204, v204
	v_pk_mul_f32 v[188:189], v[46:47], v[250:251] op_sel:[0,1] op_sel_hi:[1,1]
	v_exp_f32_e32 v201, v201
	v_pk_mul_f32 v[186:187], v[186:187], v[6:7]
	v_pk_mul_f32 v[6:7], v[92:93], v[248:249] op_sel_hi:[1,0]
	v_pk_mul_f32 v[210:211], v[82:83], v[248:249] op_sel_hi:[1,0]
	v_pk_mul_f32 v[186:187], v[186:187], v[8:9]
	v_cvt_pk_fp8_f32 v19, v218, v219 op_sel:[0,0,1]
	v_rcp_f32_e32 v208, v208
	v_pk_mul_f32 v[186:187], v[186:187], v[4:5] op_sel_hi:[1,0]
	v_exp_f32_e32 v11, v11
	v_pk_mul_f32 v[8:9], v[188:189], v[2:3] op_sel_hi:[1,0]
	v_exp_f32_e32 v15, v15
	v_pk_mul_f32 v[214:215], v[48:49], v[250:251] op_sel:[0,1] op_sel_hi:[1,1]
	v_pk_mul_f32 v[218:219], v[38:39], v[250:251] op_sel:[0,1] op_sel_hi:[1,1]
	v_med3_f32 v186, v186, s87, v227
	v_pk_mul_f32 v[6:7], v[6:7], v[24:25]
	v_pk_mul_f32 v[210:211], v[210:211], v[222:223]
	v_pk_mul_f32 v[24:25], v[84:85], v[248:249] op_sel_hi:[1,0]
	v_pk_mul_f32 v[6:7], v[6:7], v[22:23]
	v_pk_mul_f32 v[210:211], v[210:211], v[28:29]
	v_rcp_f32_e32 v27, v27
	v_pk_mul_f32 v[6:7], v[6:7], v[4:5] op_sel_hi:[1,0]
	v_pk_mul_f32 v[210:211], v[210:211], v[4:5] op_sel_hi:[1,0]
	v_exp_f32_e32 v17, v17
	v_pk_mul_f32 v[22:23], v[214:215], v[2:3] op_sel_hi:[1,0]
	v_exp_f32_e32 v8, v8
	v_pk_mul_f32 v[28:29], v[218:219], v[2:3] op_sel_hi:[1,0]
	v_pk_mul_f32 v[222:223], v[40:41], v[250:251] op_sel:[0,1] op_sel_hi:[1,1]
	v_med3_f32 v187, v187, s87, v227
	v_med3_f32 v6, v6, s87, v227
	v_med3_f32 v210, v210, s87, v227
	v_pk_mul_f32 v[24:25], v[24:25], v[30:31]
	v_rcp_f32_e32 v203, v203
	v_pk_add_f32 v[200:201], v[200:201], v[2:3] op_sel:[0,1] op_sel_hi:[1,1]
	v_pk_mul_f32 v[24:25], v[24:25], v[32:33]
	v_rcp_f32_e32 v205, v205
	v_add_u32_e32 v30, 0x1c000, v241
	v_pk_mul_f32 v[24:25], v[24:25], v[4:5] op_sel_hi:[1,0]
	v_exp_f32_e32 v22, v22
	global_store_dwordx2 v30, v[190:191], s[26:27]
	v_exp_f32_e32 v28, v28
	v_pk_mul_f32 v[30:31], v[222:223], v[2:3] op_sel_hi:[1,0]
	v_cvt_pk_fp8_f32 v32, v186, v187
	v_med3_f32 v7, v7, s87, v227
	v_med3_f32 v211, v211, s87, v227
	v_med3_f32 v24, v24, s87, v227
	v_rcp_f32_e32 v209, v209
	v_pk_add_f32 v[10:11], v[10:11], v[2:3] op_sel:[0,1] op_sel_hi:[1,1]
	v_rcp_f32_e32 v200, v200
	v_pk_add_f32 v[14:15], v[14:15], v[2:3] op_sel:[0,1] op_sel_hi:[1,1]
	v_exp_f32_e32 v30, v30
	v_pk_mul_f32 v[186:187], v[74:75], v[248:249] op_sel:[0,1] op_sel_hi:[1,1]
	v_cvt_pk_fp8_f32 v32, v6, v7 op_sel:[0,0,1]
	v_cvt_pk_fp8_f32 v33, v210, v211
	v_med3_f32 v25, v25, s87, v227
	v_rcp_f32_e32 v10, v10
	v_pk_add_f32 v[16:17], v[16:17], v[2:3] op_sel:[0,1] op_sel_hi:[1,1]
	v_rcp_f32_e32 v14, v14
	v_pk_mul_f32 v[186:187], v[186:187], v[12:13]
	v_exp_f32_e32 v9, v9
	v_pk_mul_f32 v[6:7], v[76:77], v[248:249] op_sel:[0,1] op_sel_hi:[1,1]
	v_pk_mul_f32 v[186:187], v[186:187], v[26:27]
	v_pk_mul_f32 v[12:13], v[66:67], v[248:249] op_sel:[0,1] op_sel_hi:[1,1]
	v_cvt_pk_fp8_f32 v33, v24, v25 op_sel:[0,0,1]
	v_pk_mul_f32 v[186:187], v[186:187], v[4:5] op_sel_hi:[1,0]
	v_rcp_f32_e32 v16, v16
	v_pk_mul_f32 v[6:7], v[6:7], v[192:193]
	v_exp_f32_e32 v23, v23
	v_med3_f32 v186, v186, s87, v227
	v_pk_mul_f32 v[6:7], v[6:7], v[202:203]
	v_exp_f32_e32 v29, v29
	v_pk_mul_f32 v[12:13], v[12:13], v[212:213]
	v_pk_mul_f32 v[6:7], v[6:7], v[4:5] op_sel_hi:[1,0]
	v_pk_mul_f32 v[24:25], v[68:69], v[248:249] op_sel:[0,1] op_sel_hi:[1,1]
	v_pk_mul_f32 v[12:13], v[12:13], v[204:205]
	v_rcp_f32_e32 v201, v201
	v_med3_f32 v187, v187, s87, v227
	v_pk_mul_f32 v[12:13], v[12:13], v[4:5] op_sel_hi:[1,0]
	v_exp_f32_e32 v31, v31
	v_med3_f32 v6, v6, s87, v227
	v_med3_f32 v12, v12, s87, v227
	v_pk_mul_f32 v[24:25], v[24:25], v[206:207]
	v_rcp_f32_e32 v11, v11
	v_pk_add_f32 v[8:9], v[8:9], v[2:3] op_sel:[0,1] op_sel_hi:[1,1]
	v_pk_mul_f32 v[24:25], v[24:25], v[208:209]
	v_rcp_f32_e32 v15, v15
	v_add_u32_e32 v26, 0x2a000, v241
	v_pk_mul_f32 v[24:25], v[24:25], v[4:5] op_sel_hi:[1,0]
	v_cvt_pk_fp8_f32 v186, v186, v187
	global_store_dwordx2 v26, v[18:19], s[26:27]
	v_med3_f32 v7, v7, s87, v227
	v_med3_f32 v13, v13, s87, v227
	v_med3_f32 v24, v24, s87, v227
	v_rcp_f32_e32 v17, v17
	v_pk_add_f32 v[22:23], v[22:23], v[2:3] op_sel:[0,1] op_sel_hi:[1,1]
	v_rcp_f32_e32 v8, v8
	v_pk_add_f32 v[28:29], v[28:29], v[2:3] op_sel:[0,1] op_sel_hi:[1,1]
	v_pk_mul_f32 v[18:19], v[58:59], v[250:251] op_sel_hi:[1,0]
	v_cvt_pk_fp8_f32 v186, v6, v7 op_sel:[0,0,1]
	v_cvt_pk_fp8_f32 v187, v12, v13
	v_med3_f32 v25, v25, s87, v227
	v_rcp_f32_e32 v22, v22
	v_pk_add_f32 v[30:31], v[30:31], v[2:3] op_sel:[0,1] op_sel_hi:[1,1]
	v_rcp_f32_e32 v28, v28
	v_pk_mul_f32 v[18:19], v[18:19], v[20:21]
	v_pk_mul_f32 v[6:7], v[60:61], v[250:251] op_sel_hi:[1,0]
	v_pk_mul_f32 v[12:13], v[50:51], v[250:251] op_sel_hi:[1,0]
	v_pk_mul_f32 v[18:19], v[18:19], v[200:201]
	v_cvt_pk_fp8_f32 v187, v24, v25 op_sel:[0,0,1]
	v_rcp_f32_e32 v30, v30
	v_pk_mul_f32 v[18:19], v[18:19], v[4:5] op_sel_hi:[1,0]
	v_pk_mul_f32 v[6:7], v[6:7], v[216:217]
	v_pk_mul_f32 v[12:13], v[12:13], v[236:237]
	v_med3_f32 v18, v18, s87, v227
	v_pk_mul_f32 v[6:7], v[6:7], v[10:11]
	v_pk_mul_f32 v[12:13], v[12:13], v[14:15]
	v_pk_mul_f32 v[10:11], v[52:53], v[250:251] op_sel_hi:[1,0]
	v_pk_mul_f32 v[6:7], v[6:7], v[4:5] op_sel_hi:[1,0]
	v_pk_mul_f32 v[12:13], v[12:13], v[4:5] op_sel_hi:[1,0]
	v_rcp_f32_e32 v9, v9
	v_med3_f32 v19, v19, s87, v227
	v_med3_f32 v6, v6, s87, v227
	v_med3_f32 v12, v12, s87, v227
	v_pk_mul_f32 v[10:11], v[10:11], v[220:221]
	v_rcp_f32_e32 v23, v23
	v_add_u32_e32 v14, 0x70000, v241
	v_pk_mul_f32 v[10:11], v[10:11], v[16:17]
	v_rcp_f32_e32 v29, v29
	global_store_dwordx2 v14, v[32:33], s[26:27]
	v_pk_mul_f32 v[10:11], v[10:11], v[4:5] op_sel_hi:[1,0]
	v_cvt_pk_fp8_f32 v14, v18, v19
	v_med3_f32 v7, v7, s87, v227
	v_med3_f32 v13, v13, s87, v227
	v_med3_f32 v10, v10, s87, v227
	v_rcp_f32_e32 v31, v31
	v_pk_mul_f32 v[16:17], v[42:43], v[250:251] op_sel:[0,1] op_sel_hi:[1,1]
	v_cvt_pk_fp8_f32 v14, v6, v7 op_sel:[0,0,1]
	v_cvt_pk_fp8_f32 v15, v12, v13
	v_med3_f32 v11, v11, s87, v227
	v_pk_mul_f32 v[16:17], v[16:17], v[188:189]
	v_pk_mul_f32 v[6:7], v[44:45], v[250:251] op_sel:[0,1] op_sel_hi:[1,1]
	v_pk_mul_f32 v[12:13], v[34:35], v[250:251] op_sel:[0,1] op_sel_hi:[1,1]
	v_pk_mul_f32 v[16:17], v[16:17], v[8:9]
	v_cvt_pk_fp8_f32 v15, v10, v11 op_sel:[0,0,1]
	v_pk_mul_f32 v[6:7], v[6:7], v[214:215]
	v_pk_mul_f32 v[16:17], v[16:17], v[4:5] op_sel_hi:[1,0]
	v_pk_mul_f32 v[12:13], v[12:13], v[218:219]
	v_pk_mul_f32 v[6:7], v[6:7], v[22:23]
	v_med3_f32 v16, v16, s87, v227
	v_pk_mul_f32 v[12:13], v[12:13], v[28:29]
	v_pk_mul_f32 v[6:7], v[6:7], v[4:5] op_sel_hi:[1,0]
	v_pk_mul_f32 v[8:9], v[36:37], v[250:251] op_sel:[0,1] op_sel_hi:[1,1]
	v_pk_mul_f32 v[12:13], v[12:13], v[4:5] op_sel_hi:[1,0]
	v_med3_f32 v17, v17, s87, v227
	v_med3_f32 v6, v6, s87, v227
	v_med3_f32 v12, v12, s87, v227
	v_pk_mul_f32 v[8:9], v[8:9], v[222:223]
	v_add_u32_e32 v10, 0x7e000, v241
	v_cvt_pk_fp8_f32 v16, v16, v17
	v_pk_mul_f32 v[8:9], v[8:9], v[30:31]
	global_store_dwordx2 v10, v[186:187], s[26:27]
	v_med3_f32 v7, v7, s87, v227
	v_pk_mul_f32 v[8:9], v[8:9], v[4:5] op_sel_hi:[1,0]
	v_med3_f32 v13, v13, s87, v227
	v_cvt_pk_fp8_f32 v16, v6, v7 op_sel:[0,0,1]
	v_med3_f32 v8, v8, s87, v227
	v_cvt_pk_fp8_f32 v17, v12, v13
	v_add_u32_e32 v6, 0x8c000, v241
	v_med3_f32 v9, v9, s87, v227
	v_add_u32_e32 v7, 0x9a000, v241
	global_store_dwordx2 v6, v[14:15], s[26:27]
	v_cvt_pk_fp8_f32 v17, v8, v9 op_sel:[0,0,1]
	global_store_dwordx2 v7, v[16:17], s[26:27]
	s_andn2_b64 vcc, exec, s[44:45]
	s_mov_b64 s[44:45], -1
	s_cbranch_vccnz .LBB0_832
	s_andn2_b64 vcc, exec, s[30:31]
	s_cbranch_vccnz .LBB0_831
	s_barrier
	s_branch .LBB0_831
